# QK tile blocks: both K fragments and all mask-bias reads issued up front, counted lgkmcnt (one LDS round trip per tile instead of two)
# speedup vs baseline: 1.0187x; 1.0041x over previous
.LBB1_10:
	ds_read_b128 v[4:7], v226 offset:384
	ds_read_b128 v[8:11], v226 offset:400
	ds_read_b128 v[82:85], v226 offset:416
	ds_read_b128 v[86:89], v226 offset:432
	ds_read_b128 v[12:15], v206 offset:38912
	ds_read_b128 v[244:247], v206 offset:39936
	s_waitcnt lgkmcnt(4)
	v_fma_mix_f32 v18, v162, s42, v4 op_sel:[0,0,0] op_sel_hi:[1,0,0]
	v_fma_mix_f32 v19, v162, s42, v5 op_sel:[1,0,0] op_sel_hi:[1,0,0]
	v_fma_mix_f32 v20, v163, s42, v6 op_sel:[0,0,0] op_sel_hi:[1,0,0]
	v_fma_mix_f32 v21, v163, s42, v7 op_sel:[1,0,0] op_sel_hi:[1,0,0]
	v_fma_mix_f32 v22, v164, s42, v8 op_sel:[0,0,0] op_sel_hi:[1,0,0]
	v_fma_mix_f32 v23, v164, s42, v9 op_sel:[1,0,0] op_sel_hi:[1,0,0]
	v_fma_mix_f32 v24, v165, s42, v10 op_sel:[0,0,0] op_sel_hi:[1,0,0]
	v_fma_mix_f32 v25, v165, s42, v11 op_sel:[1,0,0] op_sel_hi:[1,0,0]
	s_waitcnt lgkmcnt(2)
	v_fma_mix_f32 v26, v166, s42, v82 op_sel:[0,0,0] op_sel_hi:[1,0,0]
	v_fma_mix_f32 v27, v166, s42, v83 op_sel:[1,0,0] op_sel_hi:[1,0,0]
	v_fma_mix_f32 v28, v167, s42, v84 op_sel:[0,0,0] op_sel_hi:[1,0,0]
	v_fma_mix_f32 v29, v167, s42, v85 op_sel:[1,0,0] op_sel_hi:[1,0,0]
	v_fma_mix_f32 v30, v168, s42, v86 op_sel:[0,0,0] op_sel_hi:[1,0,0]
	v_fma_mix_f32 v31, v168, s42, v87 op_sel:[1,0,0] op_sel_hi:[1,0,0]
	v_fma_mix_f32 v32, v169, s42, v88 op_sel:[0,0,0] op_sel_hi:[1,0,0]
	v_fma_mix_f32 v33, v169, s42, v89 op_sel:[1,0,0] op_sel_hi:[1,0,0]
	s_nop 1
	s_nop 0
	s_waitcnt lgkmcnt(1)
	v_mfma_f32_32x32x16_f16 v[18:33], v[12:15], v[198:201], v[18:33]
	s_waitcnt lgkmcnt(0)
	v_mfma_f32_32x32x16_f16 v[18:33], v[244:247], v[202:205], v[18:33]

.LBB1_61:
	ds_read_b128 v[4:7], v226
	ds_read_b128 v[8:11], v226 offset:16
	ds_read_b128 v[82:85], v226 offset:32
	ds_read_b128 v[86:89], v226 offset:48
	ds_read_b128 v[12:15], v206 offset:32768
	ds_read_b128 v[244:247], v206 offset:33792
	s_waitcnt lgkmcnt(4)
	v_fma_mix_f32 v66, v190, s42, v4 op_sel:[0,0,0] op_sel_hi:[1,0,0]
	v_fma_mix_f32 v67, v190, s42, v5 op_sel:[1,0,0] op_sel_hi:[1,0,0]
	v_fma_mix_f32 v68, v191, s42, v6 op_sel:[0,0,0] op_sel_hi:[1,0,0]
	v_fma_mix_f32 v69, v191, s42, v7 op_sel:[1,0,0] op_sel_hi:[1,0,0]
	v_fma_mix_f32 v70, v192, s42, v8 op_sel:[0,0,0] op_sel_hi:[1,0,0]
	v_fma_mix_f32 v71, v192, s42, v9 op_sel:[1,0,0] op_sel_hi:[1,0,0]
	v_fma_mix_f32 v72, v193, s42, v10 op_sel:[0,0,0] op_sel_hi:[1,0,0]
	v_fma_mix_f32 v73, v193, s42, v11 op_sel:[1,0,0] op_sel_hi:[1,0,0]
	s_waitcnt lgkmcnt(2)
	v_fma_mix_f32 v74, v186, s42, v82 op_sel:[0,0,0] op_sel_hi:[1,0,0]
	v_fma_mix_f32 v75, v186, s42, v83 op_sel:[1,0,0] op_sel_hi:[1,0,0]
	v_fma_mix_f32 v76, v187, s42, v84 op_sel:[0,0,0] op_sel_hi:[1,0,0]
	v_fma_mix_f32 v77, v187, s42, v85 op_sel:[1,0,0] op_sel_hi:[1,0,0]
	v_fma_mix_f32 v78, v188, s42, v86 op_sel:[0,0,0] op_sel_hi:[1,0,0]
	v_fma_mix_f32 v79, v188, s42, v87 op_sel:[1,0,0] op_sel_hi:[1,0,0]
	v_fma_mix_f32 v80, v189, s42, v88 op_sel:[0,0,0] op_sel_hi:[1,0,0]
	v_fma_mix_f32 v81, v189, s42, v89 op_sel:[1,0,0] op_sel_hi:[1,0,0]
	s_nop 1
	s_nop 0
	s_waitcnt lgkmcnt(1)
	v_mfma_f32_32x32x16_f16 v[66:81], v[12:15], v[198:201], v[66:81]
	s_waitcnt lgkmcnt(0)
	v_mfma_f32_32x32x16_f16 v[66:81], v[244:247], v[202:205], v[66:81]
	v_cndmask_b32_e64 v1, 0, 1, s[0:1]
	v_cmp_ne_u32_e64 s[16:17], 1, v1
	s_andn2_b64 vcc, exec, s[0:1]
	s_cbranch_vccnz .LBB1_8
.LBB1_62:
	ds_read_b128 v[4:7], v226 offset:128
	ds_read_b128 v[8:11], v226 offset:144
	ds_read_b128 v[82:85], v226 offset:160
	ds_read_b128 v[86:89], v226 offset:176
	ds_read_b128 v[12:15], v206 offset:34816
	ds_read_b128 v[244:247], v206 offset:35840
	s_waitcnt lgkmcnt(4)
	v_fma_mix_f32 v50, v182, s42, v4 op_sel:[0,0,0] op_sel_hi:[1,0,0]
	v_fma_mix_f32 v51, v182, s42, v5 op_sel:[1,0,0] op_sel_hi:[1,0,0]
	v_fma_mix_f32 v52, v183, s42, v6 op_sel:[0,0,0] op_sel_hi:[1,0,0]
	v_fma_mix_f32 v53, v183, s42, v7 op_sel:[1,0,0] op_sel_hi:[1,0,0]
	v_fma_mix_f32 v54, v184, s42, v8 op_sel:[0,0,0] op_sel_hi:[1,0,0]
	v_fma_mix_f32 v55, v184, s42, v9 op_sel:[1,0,0] op_sel_hi:[1,0,0]
	v_fma_mix_f32 v56, v185, s42, v10 op_sel:[0,0,0] op_sel_hi:[1,0,0]
	v_fma_mix_f32 v57, v185, s42, v11 op_sel:[1,0,0] op_sel_hi:[1,0,0]
	s_waitcnt lgkmcnt(2)
	v_fma_mix_f32 v58, v178, s42, v82 op_sel:[0,0,0] op_sel_hi:[1,0,0]
	v_fma_mix_f32 v59, v178, s42, v83 op_sel:[1,0,0] op_sel_hi:[1,0,0]
	v_fma_mix_f32 v60, v179, s42, v84 op_sel:[0,0,0] op_sel_hi:[1,0,0]
	v_fma_mix_f32 v61, v179, s42, v85 op_sel:[1,0,0] op_sel_hi:[1,0,0]
	v_fma_mix_f32 v62, v180, s42, v86 op_sel:[0,0,0] op_sel_hi:[1,0,0]
	v_fma_mix_f32 v63, v180, s42, v87 op_sel:[1,0,0] op_sel_hi:[1,0,0]
	v_fma_mix_f32 v64, v181, s42, v88 op_sel:[0,0,0] op_sel_hi:[1,0,0]
	v_fma_mix_f32 v65, v181, s42, v89 op_sel:[1,0,0] op_sel_hi:[1,0,0]
	s_nop 1
	s_nop 0
	s_waitcnt lgkmcnt(1)
	v_mfma_f32_32x32x16_f16 v[50:65], v[12:15], v[198:201], v[50:65]
	s_waitcnt lgkmcnt(0)
	v_mfma_f32_32x32x16_f16 v[50:65], v[244:247], v[202:205], v[50:65]
	v_cndmask_b32_e64 v1, 0, 1, s[6:7]
	v_cmp_ne_u32_e64 s[18:19], 1, v1
	s_andn2_b64 vcc, exec, s[6:7]
	s_cbranch_vccnz .LBB1_9
.LBB1_63:
	ds_read_b128 v[4:7], v226 offset:256
	ds_read_b128 v[8:11], v226 offset:272
	ds_read_b128 v[82:85], v226 offset:288
	ds_read_b128 v[86:89], v226 offset:304
	ds_read_b128 v[12:15], v206 offset:36864
	ds_read_b128 v[244:247], v206 offset:37888
	s_waitcnt lgkmcnt(4)
	v_fma_mix_f32 v34, v170, s42, v4 op_sel:[0,0,0] op_sel_hi:[1,0,0]
	v_fma_mix_f32 v35, v170, s42, v5 op_sel:[1,0,0] op_sel_hi:[1,0,0]
	v_fma_mix_f32 v36, v171, s42, v6 op_sel:[0,0,0] op_sel_hi:[1,0,0]
	v_fma_mix_f32 v37, v171, s42, v7 op_sel:[1,0,0] op_sel_hi:[1,0,0]
	v_fma_mix_f32 v38, v172, s42, v8 op_sel:[0,0,0] op_sel_hi:[1,0,0]
	v_fma_mix_f32 v39, v172, s42, v9 op_sel:[1,0,0] op_sel_hi:[1,0,0]
	v_fma_mix_f32 v40, v173, s42, v10 op_sel:[0,0,0] op_sel_hi:[1,0,0]
	v_fma_mix_f32 v41, v173, s42, v11 op_sel:[1,0,0] op_sel_hi:[1,0,0]
	s_waitcnt lgkmcnt(2)
	v_fma_mix_f32 v42, v174, s42, v82 op_sel:[0,0,0] op_sel_hi:[1,0,0]
	v_fma_mix_f32 v43, v174, s42, v83 op_sel:[1,0,0] op_sel_hi:[1,0,0]
	v_fma_mix_f32 v44, v175, s42, v84 op_sel:[0,0,0] op_sel_hi:[1,0,0]
	v_fma_mix_f32 v45, v175, s42, v85 op_sel:[1,0,0] op_sel_hi:[1,0,0]
	v_fma_mix_f32 v46, v176, s42, v86 op_sel:[0,0,0] op_sel_hi:[1,0,0]
	v_fma_mix_f32 v47, v176, s42, v87 op_sel:[1,0,0] op_sel_hi:[1,0,0]
	v_fma_mix_f32 v48, v177, s42, v88 op_sel:[0,0,0] op_sel_hi:[1,0,0]
	v_fma_mix_f32 v49, v177, s42, v89 op_sel:[1,0,0] op_sel_hi:[1,0,0]
	s_nop 1
	s_nop 0
	s_waitcnt lgkmcnt(1)
	v_mfma_f32_32x32x16_f16 v[34:49], v[12:15], v[198:201], v[34:49]
	s_waitcnt lgkmcnt(0)
	v_mfma_f32_32x32x16_f16 v[34:49], v[244:247], v[202:205], v[34:49]
	v_cndmask_b32_e64 v1, 0, 1, s[4:5]
	v_cmp_ne_u32_e64 s[20:21], 1, v1
	s_andn2_b64 vcc, exec, s[4:5]
	s_cbranch_vccz .LBB1_10
	s_branch .LBB1_11

.LBB1_71:
	s_waitcnt vmcnt(4)
	ds_read_b128 v[4:7], v226 offset:512
	ds_read_b128 v[8:11], v226 offset:528
	ds_read_b128 v[114:117], v226 offset:544
	ds_read_b128 v[118:121], v226 offset:560
	ds_read_b128 v[12:15], v206 offset:40960
	ds_read_b128 v[244:247], v206 offset:41984
	s_waitcnt lgkmcnt(4)
	v_fma_mix_f32 v66, v190, s42, v4 op_sel:[0,0,0] op_sel_hi:[1,0,0]
	v_fma_mix_f32 v67, v190, s42, v5 op_sel:[1,0,0] op_sel_hi:[1,0,0]
	v_fma_mix_f32 v68, v191, s42, v6 op_sel:[0,0,0] op_sel_hi:[1,0,0]
	v_fma_mix_f32 v69, v191, s42, v7 op_sel:[1,0,0] op_sel_hi:[1,0,0]
	v_fma_mix_f32 v70, v192, s42, v8 op_sel:[0,0,0] op_sel_hi:[1,0,0]
	v_fma_mix_f32 v71, v192, s42, v9 op_sel:[1,0,0] op_sel_hi:[1,0,0]
	v_fma_mix_f32 v72, v193, s42, v10 op_sel:[0,0,0] op_sel_hi:[1,0,0]
	v_fma_mix_f32 v73, v193, s42, v11 op_sel:[1,0,0] op_sel_hi:[1,0,0]
	s_waitcnt lgkmcnt(2)
	v_fma_mix_f32 v74, v186, s42, v114 op_sel:[0,0,0] op_sel_hi:[1,0,0]
	v_fma_mix_f32 v75, v186, s42, v115 op_sel:[1,0,0] op_sel_hi:[1,0,0]
	v_fma_mix_f32 v76, v187, s42, v116 op_sel:[0,0,0] op_sel_hi:[1,0,0]
	v_fma_mix_f32 v77, v187, s42, v117 op_sel:[1,0,0] op_sel_hi:[1,0,0]
	v_fma_mix_f32 v78, v188, s42, v118 op_sel:[0,0,0] op_sel_hi:[1,0,0]
	v_fma_mix_f32 v79, v188, s42, v119 op_sel:[1,0,0] op_sel_hi:[1,0,0]
	v_fma_mix_f32 v80, v189, s42, v120 op_sel:[0,0,0] op_sel_hi:[1,0,0]
	v_fma_mix_f32 v81, v189, s42, v121 op_sel:[1,0,0] op_sel_hi:[1,0,0]
	s_nop 1
	s_nop 0
	s_waitcnt lgkmcnt(1)
	v_mfma_f32_32x32x16_f16 v[66:81], v[12:15], v[198:201], v[66:81]
	s_waitcnt lgkmcnt(0)
	v_mfma_f32_32x32x16_f16 v[66:81], v[244:247], v[202:205], v[66:81]
	v_cndmask_b32_e64 v1, 0, 1, s[8:9]
	v_cmp_ne_u32_e64 s[20:21], 1, v1
	s_andn2_b64 vcc, exec, s[8:9]
	s_cbranch_vccnz .LBB1_34
.LBB1_72:
	s_waitcnt vmcnt(4)
	ds_read_b128 v[4:7], v226 offset:640
	ds_read_b128 v[8:11], v226 offset:656
	ds_read_b128 v[114:117], v226 offset:672
	ds_read_b128 v[118:121], v226 offset:688
	ds_read_b128 v[12:15], v206 offset:43008
	ds_read_b128 v[244:247], v206 offset:44032
	s_waitcnt lgkmcnt(4)
	v_fma_mix_f32 v50, v182, s42, v4 op_sel:[0,0,0] op_sel_hi:[1,0,0]
	v_fma_mix_f32 v51, v182, s42, v5 op_sel:[1,0,0] op_sel_hi:[1,0,0]
	v_fma_mix_f32 v52, v183, s42, v6 op_sel:[0,0,0] op_sel_hi:[1,0,0]
	v_fma_mix_f32 v53, v183, s42, v7 op_sel:[1,0,0] op_sel_hi:[1,0,0]
	v_fma_mix_f32 v54, v184, s42, v8 op_sel:[0,0,0] op_sel_hi:[1,0,0]
	v_fma_mix_f32 v55, v184, s42, v9 op_sel:[1,0,0] op_sel_hi:[1,0,0]
	v_fma_mix_f32 v56, v185, s42, v10 op_sel:[0,0,0] op_sel_hi:[1,0,0]
	v_fma_mix_f32 v57, v185, s42, v11 op_sel:[1,0,0] op_sel_hi:[1,0,0]
	s_waitcnt lgkmcnt(2)
	v_fma_mix_f32 v58, v178, s42, v114 op_sel:[0,0,0] op_sel_hi:[1,0,0]
	v_fma_mix_f32 v59, v178, s42, v115 op_sel:[1,0,0] op_sel_hi:[1,0,0]
	v_fma_mix_f32 v60, v179, s42, v116 op_sel:[0,0,0] op_sel_hi:[1,0,0]
	v_fma_mix_f32 v61, v179, s42, v117 op_sel:[1,0,0] op_sel_hi:[1,0,0]
	v_fma_mix_f32 v62, v180, s42, v118 op_sel:[0,0,0] op_sel_hi:[1,0,0]
	v_fma_mix_f32 v63, v180, s42, v119 op_sel:[1,0,0] op_sel_hi:[1,0,0]
	v_fma_mix_f32 v64, v181, s42, v120 op_sel:[0,0,0] op_sel_hi:[1,0,0]
	v_fma_mix_f32 v65, v181, s42, v121 op_sel:[1,0,0] op_sel_hi:[1,0,0]
	s_nop 1
	s_nop 0
	s_waitcnt lgkmcnt(1)
	v_mfma_f32_32x32x16_f16 v[50:65], v[12:15], v[198:201], v[50:65]
	s_waitcnt lgkmcnt(0)
	v_mfma_f32_32x32x16_f16 v[50:65], v[244:247], v[202:205], v[50:65]
	v_cndmask_b32_e64 v1, 0, 1, s[14:15]
	v_cmp_ne_u32_e64 s[22:23], 1, v1
	s_andn2_b64 vcc, exec, s[14:15]
	s_cbranch_vccnz .LBB1_35
.LBB1_73:
	s_waitcnt vmcnt(4)
	ds_read_b128 v[4:7], v226 offset:768
	ds_read_b128 v[8:11], v226 offset:784
	ds_read_b128 v[114:117], v226 offset:800
	ds_read_b128 v[118:121], v226 offset:816
	ds_read_b128 v[12:15], v206 offset:45056
	ds_read_b128 v[244:247], v206 offset:46080
	s_waitcnt lgkmcnt(4)
	v_fma_mix_f32 v34, v170, s42, v4 op_sel:[0,0,0] op_sel_hi:[1,0,0]
	v_fma_mix_f32 v35, v170, s42, v5 op_sel:[1,0,0] op_sel_hi:[1,0,0]
	v_fma_mix_f32 v36, v171, s42, v6 op_sel:[0,0,0] op_sel_hi:[1,0,0]
	v_fma_mix_f32 v37, v171, s42, v7 op_sel:[1,0,0] op_sel_hi:[1,0,0]
	v_fma_mix_f32 v38, v172, s42, v8 op_sel:[0,0,0] op_sel_hi:[1,0,0]
	v_fma_mix_f32 v39, v172, s42, v9 op_sel:[1,0,0] op_sel_hi:[1,0,0]
	v_fma_mix_f32 v40, v173, s42, v10 op_sel:[0,0,0] op_sel_hi:[1,0,0]
	v_fma_mix_f32 v41, v173, s42, v11 op_sel:[1,0,0] op_sel_hi:[1,0,0]
	s_waitcnt lgkmcnt(2)
	v_fma_mix_f32 v42, v174, s42, v114 op_sel:[0,0,0] op_sel_hi:[1,0,0]
	v_fma_mix_f32 v43, v174, s42, v115 op_sel:[1,0,0] op_sel_hi:[1,0,0]
	v_fma_mix_f32 v44, v175, s42, v116 op_sel:[0,0,0] op_sel_hi:[1,0,0]
	v_fma_mix_f32 v45, v175, s42, v117 op_sel:[1,0,0] op_sel_hi:[1,0,0]
	v_fma_mix_f32 v46, v176, s42, v118 op_sel:[0,0,0] op_sel_hi:[1,0,0]
	v_fma_mix_f32 v47, v176, s42, v119 op_sel:[1,0,0] op_sel_hi:[1,0,0]
	v_fma_mix_f32 v48, v177, s42, v120 op_sel:[0,0,0] op_sel_hi:[1,0,0]
	v_fma_mix_f32 v49, v177, s42, v121 op_sel:[1,0,0] op_sel_hi:[1,0,0]
	s_nop 1
	s_nop 0
	s_waitcnt lgkmcnt(1)
	v_mfma_f32_32x32x16_f16 v[34:49], v[12:15], v[198:201], v[34:49]
	s_waitcnt lgkmcnt(0)
	v_mfma_f32_32x32x16_f16 v[34:49], v[244:247], v[202:205], v[34:49]
	v_cndmask_b32_e64 v1, 0, 1, s[12:13]
	v_cmp_ne_u32_e64 s[24:25], 1, v1
	s_andn2_b64 vcc, exec, s[12:13]
	s_cbranch_vccnz .LBB1_36
.LBB1_74:
	s_waitcnt vmcnt(4)
	ds_read_b128 v[4:7], v226 offset:896
	ds_read_b128 v[8:11], v226 offset:912
	ds_read_b128 v[114:117], v226 offset:928
	ds_read_b128 v[118:121], v226 offset:944
	ds_read_b128 v[12:15], v206 offset:47104
	ds_read_b128 v[244:247], v206 offset:48128
	s_waitcnt lgkmcnt(4)
	v_fma_mix_f32 v18, v162, s42, v4 op_sel:[0,0,0] op_sel_hi:[1,0,0]
	v_fma_mix_f32 v19, v162, s42, v5 op_sel:[1,0,0] op_sel_hi:[1,0,0]
	v_fma_mix_f32 v20, v163, s42, v6 op_sel:[0,0,0] op_sel_hi:[1,0,0]
	v_fma_mix_f32 v21, v163, s42, v7 op_sel:[1,0,0] op_sel_hi:[1,0,0]
	v_fma_mix_f32 v22, v164, s42, v8 op_sel:[0,0,0] op_sel_hi:[1,0,0]
	v_fma_mix_f32 v23, v164, s42, v9 op_sel:[1,0,0] op_sel_hi:[1,0,0]
	v_fma_mix_f32 v24, v165, s42, v10 op_sel:[0,0,0] op_sel_hi:[1,0,0]
	v_fma_mix_f32 v25, v165, s42, v11 op_sel:[1,0,0] op_sel_hi:[1,0,0]
	s_waitcnt lgkmcnt(2)
	v_fma_mix_f32 v26, v166, s42, v114 op_sel:[0,0,0] op_sel_hi:[1,0,0]
	v_fma_mix_f32 v27, v166, s42, v115 op_sel:[1,0,0] op_sel_hi:[1,0,0]
	v_fma_mix_f32 v28, v167, s42, v116 op_sel:[0,0,0] op_sel_hi:[1,0,0]
	v_fma_mix_f32 v29, v167, s42, v117 op_sel:[1,0,0] op_sel_hi:[1,0,0]
	v_fma_mix_f32 v30, v168, s42, v118 op_sel:[0,0,0] op_sel_hi:[1,0,0]
	v_fma_mix_f32 v31, v168, s42, v119 op_sel:[1,0,0] op_sel_hi:[1,0,0]
	v_fma_mix_f32 v32, v169, s42, v120 op_sel:[0,0,0] op_sel_hi:[1,0,0]
	v_fma_mix_f32 v33, v169, s42, v121 op_sel:[1,0,0] op_sel_hi:[1,0,0]
	s_nop 1
	s_nop 0
	s_waitcnt lgkmcnt(1)
	v_mfma_f32_32x32x16_f16 v[18:33], v[12:15], v[198:201], v[18:33]
	s_waitcnt lgkmcnt(0)
	v_mfma_f32_32x32x16_f16 v[18:33], v[244:247], v[202:205], v[18:33]
	v_cndmask_b32_e64 v1, 0, 1, s[52:53]
	v_cmp_ne_u32_e64 s[16:17], 1, v1
	s_andn2_b64 vcc, exec, s[52:53]
	s_cbranch_vccz .LBB1_37
	s_branch .LBB1_38
